# nt11 + GEMM3: each unit's residual x tile touched at unit start (prefetch under the K-loop)
# speedup vs baseline: 1.0041x; 1.0041x over previous
;     __host__ __device__ bool next(int i, Unit& u) const {
;         const long L = (long)i * G + c; if (L >= nwg) return false;
;         int wgid = (int)L; { const int q = nwg / NXCD, r = nwg % NXCD, xcd = wgid % NXCD, off = wgid / NXCD; wgid = (xcd < r ? xcd * (q + 1) : r * (q + 1) + (xcd - r) * q) + off; }
;         const int nig = WGM * nN, gid = wgid / nig, fm = gid * WGM, gsz = (nM - fm) < WGM ? (nM - fm) : WGM;
;         u.pm = fm + ((wgid % nig) % gsz); u.pn = (wgid % nig) / gsz; return true;
;     }
.LBB0_607:
	s_lshl_b32 s98, s29, 22
	s_lshl_b32 s99, s28, 10
	s_add_u32 s98, s98, s99
	v_readlane_b32 s99, v255, 10
	s_lshl_b32 s99, s99, 19
	s_add_u32 s98, s98, s99
	s_add_u32 s98, s8, s98
	s_addc_u32 s99, s9, 0
	v_lshrrev_b32_e32 v250, 3, v202
	v_and_b32_e32 v251, 7, v202
	v_lshlrev_b32_e32 v250, 14, v250
	v_lshl_or_b32 v250, v251, 7, v250
	s_nop 0
	global_load_dword v251, v250, s[98:99]
	s_add_u32 s98, s98, 0x20000
	s_addc_u32 s99, s99, 0
	global_load_dword v251, v250, s[98:99]
	s_add_u32 s98, s98, 0x20000
	s_addc_u32 s99, s99, 0
	global_load_dword v251, v250, s[98:99]
	s_add_u32 s98, s98, 0x20000
	s_addc_u32 s99, s99, 0
	global_load_dword v251, v250, s[98:99]
	s_add_i32 s37, s37, 1
	v_readlane_b32 s22, v255, 2
	s_mul_i32 s4, s37, s46
	s_mul_hi_u32 s5, s37, s22
	s_add_i32 s5, s5, s4
	s_mul_i32 s4, s37, s22
	s_add_u32 s22, s4, s2
	s_addc_u32 s23, s5, s47
	v_cmp_gt_i64_e32 vcc, s[22:23], v[164:165]
	v_cmp_lt_i64_e64 s[4:5], s[22:23], v[162:163]
	s_cbranch_vccnz .LBB0_613
	s_ashr_i32 s23, s22, 31
	s_lshr_b32 s23, s23, 29
	s_add_i32 s58, s22, s23
	s_and_b32 s23, s58, -8
	s_sub_i32 s59, s22, s23
	s_cmp_gt_i32 s59, -1
	s_mov_b64 s[22:23], -1
	s_cbranch_scc0 .LBB0_610
	s_lshl_b32 s60, s59, 6
	s_mov_b64 s[22:23], 0

.LBB0_613:
	s_mul_i32 s60, s59, 0x108000
	s_and_b64 s[22:23], s[4:5], exec
	s_mul_i32 s61, s58, 0x108000
	v_mov_b32_e32 v2, 0
	s_cselect_b32 s68, s60, s70
	s_cselect_b32 s69, s61, s71
	s_add_i32 s70, s70, 0x84080
	s_addk_i32 s71, 0x100
	s_mov_b32 s72, -2
	s_waitcnt lgkmcnt(0)
	v_mov_b32_e32 v3, v2
	v_mov_b32_e32 v4, v2
	v_mov_b32_e32 v5, v2
	v_mov_b32_e32 v6, v2
	v_mov_b32_e32 v7, v2
	v_mov_b32_e32 v8, v2
	v_mov_b32_e32 v9, v2
	s_waitcnt vmcnt(21)
	v_mov_b32_e32 v18, v2
	v_mov_b32_e32 v19, v2
	v_mov_b32_e32 v20, v2
	v_mov_b32_e32 v21, v2
	v_mov_b32_e32 v22, v2
	v_mov_b32_e32 v23, v2
	v_mov_b32_e32 v24, v2
	v_mov_b32_e32 v25, v2
	v_mov_b32_e32 v34, v2
	v_mov_b32_e32 v35, v2
	v_mov_b32_e32 v36, v2
	v_mov_b32_e32 v37, v2
	v_mov_b32_e32 v38, v2
	v_mov_b32_e32 v39, v2
	v_mov_b32_e32 v40, v2
	v_mov_b32_e32 v41, v2
	s_waitcnt vmcnt(20)
	v_mov_b32_e32 v54, v2
	v_mov_b32_e32 v55, v2
	v_mov_b32_e32 v56, v2
	v_mov_b32_e32 v57, v2
	v_mov_b32_e32 v58, v2
	v_mov_b32_e32 v59, v2
	v_mov_b32_e32 v60, v2
	v_mov_b32_e32 v61, v2
	v_mov_b32_e32 v10, v2
	v_mov_b32_e32 v11, v2
	v_mov_b32_e32 v12, v2
	v_mov_b32_e32 v13, v2
	v_mov_b32_e32 v14, v2
	v_mov_b32_e32 v15, v2
	v_mov_b32_e32 v16, v2
	v_mov_b32_e32 v17, v2
	s_waitcnt vmcnt(19)
	v_mov_b32_e32 v26, v2
	v_mov_b32_e32 v27, v2
	v_mov_b32_e32 v28, v2
	v_mov_b32_e32 v29, v2
	v_mov_b32_e32 v30, v2
	v_mov_b32_e32 v31, v2
	v_mov_b32_e32 v32, v2
	v_mov_b32_e32 v33, v2
	v_mov_b32_e32 v42, v2
	v_mov_b32_e32 v43, v2
	v_mov_b32_e32 v44, v2
	v_mov_b32_e32 v45, v2
	v_mov_b32_e32 v46, v2
	v_mov_b32_e32 v47, v2
	v_mov_b32_e32 v48, v2
	v_mov_b32_e32 v49, v2
	v_mov_b32_e32 v70, v2
	v_mov_b32_e32 v71, v2
	v_mov_b32_e32 v72, v2
	v_mov_b32_e32 v73, v2
	v_mov_b32_e32 v78, v2
	v_mov_b32_e32 v79, v2
	v_mov_b32_e32 v80, v2
	v_mov_b32_e32 v81, v2
	v_mov_b32_e32 v82, v2
	v_mov_b32_e32 v83, v2
	v_mov_b32_e32 v84, v2
	v_mov_b32_e32 v85, v2
	v_mov_b32_e32 v86, v2
	v_mov_b32_e32 v87, v2
	v_mov_b32_e32 v88, v2
	v_mov_b32_e32 v89, v2
	v_mov_b32_e32 v98, v2
	v_mov_b32_e32 v99, v2
	v_mov_b32_e32 v100, v2
	v_mov_b32_e32 v101, v2
	v_mov_b32_e32 v102, v2
	v_mov_b32_e32 v103, v2
	v_mov_b32_e32 v104, v2
	v_mov_b32_e32 v105, v2
	v_mov_b32_e32 v114, v2
	v_mov_b32_e32 v115, v2
	v_mov_b32_e32 v116, v2
	v_mov_b32_e32 v117, v2
	v_mov_b32_e32 v118, v2
	v_mov_b32_e32 v119, v2
	v_mov_b32_e32 v120, v2
	v_mov_b32_e32 v121, v2
	v_mov_b32_e32 v130, v2
	v_mov_b32_e32 v131, v2
	v_mov_b32_e32 v132, v2
	v_mov_b32_e32 v133, v2
	v_mov_b32_e32 v134, v2
	v_mov_b32_e32 v135, v2
	v_mov_b32_e32 v136, v2
	v_mov_b32_e32 v137, v2
	v_mov_b32_e32 v90, v2
	v_mov_b32_e32 v91, v2
	v_mov_b32_e32 v92, v2
	v_mov_b32_e32 v93, v2
	v_mov_b32_e32 v94, v2
	v_mov_b32_e32 v95, v2
	v_mov_b32_e32 v96, v2
	v_mov_b32_e32 v97, v2
	v_mov_b32_e32 v106, v2
	v_mov_b32_e32 v107, v2
	v_mov_b32_e32 v108, v2
	v_mov_b32_e32 v109, v2
	v_mov_b32_e32 v110, v2
	v_mov_b32_e32 v111, v2
	v_mov_b32_e32 v112, v2
	v_mov_b32_e32 v113, v2
	v_mov_b32_e32 v122, v2
	v_mov_b32_e32 v123, v2
	v_mov_b32_e32 v124, v2
	v_mov_b32_e32 v125, v2
	v_mov_b32_e32 v126, v2
	v_mov_b32_e32 v127, v2
	v_mov_b32_e32 v128, v2
	v_mov_b32_e32 v129, v2
	v_mov_b32_e32 v50, v2
	v_mov_b32_e32 v51, v2
	v_mov_b32_e32 v52, v2
	v_mov_b32_e32 v53, v2
	v_mov_b32_e32 v62, v2
	v_mov_b32_e32 v63, v2
	v_mov_b32_e32 v64, v2
	v_mov_b32_e32 v65, v2
